# phase 3: second-half B fragment reads issued under the first half's MFMAs
# baseline (speedup 1.0000x reference)
.LBB1_4:
	s_or_b64 exec, exec, s[4:5]
	v_lshl_or_b32 v4, v27, 1, v96
	v_lshl_or_b32 v3, v4, 7, v3
	v_or_b32_e32 v5, 0x23600, v3
	v_or_b32_e32 v3, 0x23640, v3
	s_waitcnt lgkmcnt(0)
	s_barrier
	ds_read_b32 v5, v5
	ds_read_b32 v3, v3
	v_mad_u32_u24 v4, v4, s7, v13
	v_lshl_add_u32 v4, v119, 4, v4
	v_or_b32_e32 v6, 0x20000, v4
	ds_read_b128 v[16:19], v6
	s_waitcnt lgkmcnt(1)
	v_add_f32_e32 v3, v5, v3
	v_add_u32_e32 v5, 0x20020, v4
	v_add_u32_e32 v6, 0x20040, v4
	ds_read_b128 v[112:115], v5
	ds_read_b128 v[108:111], v6
	v_add_u32_e32 v5, 0x20060, v4
	v_add_u32_e32 v6, 0x20080, v4
	v_lshlrev_b32_e32 v7, 1, v101
	ds_read_b128 v[104:107], v5
	ds_read_b128 v[96:99], v6
	v_lshrrev_b32_e32 v5, 2, v100
	v_or_b32_e32 v6, v28, v125
	v_and_b32_e32 v7, 2, v7
	v_bfe_u32 v8, v0, 1, 1
	v_and_b32_e32 v164, 8, v121
	v_bfe_i32 v9, v0, 7, 1
	v_or3_b32 v8, v8, v7, v164
	v_and_b32_e32 v0, 12, v0
	v_add_lshl_u32 v10, v6, v5, 8
	v_or_b32_e32 v5, v6, v5
	v_and_b32_e32 v9, 0xc000, v9
	v_lshlrev_b32_e32 v12, 8, v5
	v_bitop3_b32 v5, v0, v8, v124 bitop3:0x36
	v_lshl_or_b32 v13, v5, 4, v9
	v_bitop3_b32 v6, v0, v8, v2 bitop3:0x36
	v_or_b32_e32 v15, 0x1000, v12
	v_lshl_or_b32 v14, v6, 4, v9
	v_add_u32_e32 v7, v13, v15
	v_or_b32_e32 v24, 0x1400, v12
	v_or_b32_e32 v20, v7, v1
	v_add_u32_e32 v7, v14, v24
	v_add_u32_e32 v25, 0x2000, v10
	v_add_u32_e32 v5, v13, v12
	v_add_u32_e32 v6, v14, v12
	v_or_b32_e32 v22, v7, v1
	v_add_u32_e32 v7, v13, v25
	v_add_u32_e32 v150, 0x3000, v10
	v_or_b32_e32 v8, 4, v8
	v_add_u32_e32 v4, 0x200a0, v4
	v_or_b32_e32 v5, v5, v1
	v_or_b32_e32 v6, v6, v1
	v_or_b32_e32 v27, v7, v1
	v_add_u32_e32 v31, v13, v150
	v_add_u32_e32 v151, 0x3400, v10
	v_bitop3_b32 v124, v0, v8, v124 bitop3:0x36
	v_bitop3_b32 v0, v0, v8, v2 bitop3:0x36
	ds_read_b128 v[100:103], v4
	ds_read_b64_tr_b16 v[4:5], v5
	ds_read_b64_tr_b16 v[6:7], v6 offset:1024
	ds_read_b64_tr_b16 v[20:21], v20
	ds_read_b64_tr_b16 v[22:23], v22
	ds_read_b64_tr_b16 v[28:29], v27
	v_add_u32_e32 v27, 0x2400, v10
	v_or_b32_e32 v128, v31, v1
	v_add_u32_e32 v31, v14, v151
	v_add_u32_e32 v152, 0x4000, v10
	v_add_u32_e32 v158, 0x4400, v10
	v_lshl_or_b32 v124, v124, 4, v9
	v_lshl_or_b32 v0, v0, 4, v9
	v_add_u32_e32 v11, 0x5000, v10
	v_add_u32_e32 v30, v14, v27
	v_or_b32_e32 v130, v31, v1
	v_add_u32_e32 v31, v13, v152
	v_add_u32_e32 v134, v14, v158
	v_add_u32_e32 v10, 0x5400, v10
	v_add_u32_e32 v135, v124, v12
	v_add_u32_e32 v2, v0, v12
	v_add_u32_e32 v8, v124, v15
	v_or_b32_e32 v30, v30, v1
	v_or_b32_e32 v132, v31, v1
	v_or_b32_e32 v134, v134, v1
	v_add_u32_e32 v13, v13, v11
	v_add_u32_e32 v14, v14, v10
	v_or_b32_e32 v140, v135, v1
	v_or_b32_e32 v2, v2, v1
	v_or_b32_e32 v8, v8, v1
	v_add_u32_e32 v9, v0, v24
	v_add_u32_e32 v12, v124, v25
	ds_read_b64_tr_b16 v[30:31], v30
	ds_read_b64_tr_b16 v[128:129], v128
	ds_read_b64_tr_b16 v[130:131], v130
	ds_read_b64_tr_b16 v[132:133], v132
	v_or_b32_e32 v13, v13, v1
	v_or_b32_e32 v14, v14, v1
	ds_read_b64_tr_b16 v[134:135], v134
	ds_read_b64_tr_b16 v[136:137], v13
	ds_read_b64_tr_b16 v[138:139], v14
	ds_read_b64_tr_b16 v[140:141], v140
	v_or_b32_e32 v9, v9, v1
	v_or_b32_e32 v12, v12, v1
	ds_read_b64_tr_b16 v[142:143], v2 offset:1024
	ds_read_b64_tr_b16 v[144:145], v8
	ds_read_b64_tr_b16 v[146:147], v9
	ds_read_b64_tr_b16 v[148:149], v12
	v_add_u32_e32 v2, v0, v27
	v_add_u32_e32 v8, v124, v150
	v_or_b32_e32 v2, v2, v1
	v_or_b32_e32 v8, v8, v1
	v_add_u32_e32 v9, v0, v151
	v_add_u32_e32 v12, v124, v152
	v_or_b32_e32 v9, v9, v1
	v_or_b32_e32 v12, v12, v1
	ds_read_b64_tr_b16 v[150:151], v2
	ds_read_b64_tr_b16 v[152:153], v8
	ds_read_b64_tr_b16 v[154:155], v9
	ds_read_b64_tr_b16 v[156:157], v12
	v_add_u32_e32 v2, v0, v158
	v_add_u32_e32 v8, v124, v11
	v_add_u32_e32 v0, v0, v10
	v_or_b32_e32 v2, v2, v1
	v_or_b32_e32 v8, v8, v1
	v_or_b32_e32 v0, v0, v1
	v_div_scale_f32 v1, s[8:9], v3, v3, 1.0
	v_rcp_f32_e32 v9, v1
	ds_read_b64_tr_b16 v[158:159], v2
	ds_read_b64_tr_b16 v[160:161], v8
	ds_read_b64_tr_b16 v[162:163], v0
	s_mov_b32 s4, 0xc000
	s_movk_i32 s5, 0x4000
	v_fma_f32 v0, -v1, v9, 1.0
	v_fmac_f32_e32 v9, v0, v9
	v_div_scale_f32 v0, vcc, 1.0, v3, 1.0
	v_mul_f32_e32 v2, v0, v9
	v_fma_f32 v8, -v1, v2, v0
	v_fmac_f32_e32 v2, v8, v9
	v_fma_f32 v0, -v1, v2, v0
	v_div_fmas_f32 v0, v0, v9, v2
	v_div_fixup_f32 v124, v0, v3, 1.0
	s_waitcnt lgkmcnt(14)
	v_mfma_f32_32x32x16_f16 v[0:15], v[4:7], v[16:19], 0
	s_mov_b32 s7, 0x18000
	v_lshlrev_b32_e32 v172, 2, v126
	v_mov_b32_e32 v173, 0
	v_mfma_f32_32x32x16_f16 v[0:15], v[20:23], v[112:115], v[0:15]
	v_or_b32_e32 v20, v26, v116
	v_and_b32_e32 v21, 0x4000, v118
	v_lshl_or_b32 v20, v20, 8, v21
	v_bitop3_b32 v118, v121, v120, 8 bitop3:0x6c
	v_or3_b32 v121, v20, v125, s7
	v_mfma_f32_32x32x16_f16 v[0:15], v[28:31], v[108:111], v[0:15]
	v_mfma_f32_32x32x16_f16 v[0:15], v[128:131], v[104:107], v[0:15]
	v_mfma_f32_32x32x16_f16 v[0:15], v[132:135], v[96:99], v[0:15]
	s_waitcnt lgkmcnt(12)
	v_mfma_f32_32x32x16_f16 v[0:15], v[136:139], v[100:103], v[0:15]
	s_nop 11
	v_fma_mixlo_f16 v20, v124, v0, 0
	v_mov_b32_e32 v0, v1
	v_mov_b32_e32 v1, v2
	v_pk_mul_f32 v[0:1], v[124:125], v[0:1] op_sel_hi:[0,1]
	v_cvt_pk_f16_f32 v1, v0, v1
	v_pack_b32_f16 v0, v20, v1
	s_waitcnt lgkmcnt(10)
	v_mfma_f32_32x32x16_f16 v[16:31], v[140:143], v[16:19], 0
	v_fma_mixlo_f16 v2, v124, v3, 0
	v_alignbit_b32 v1, v2, v1, 16
	v_lshl_or_b32 v2, v118, 4, v121
	ds_write_b64 v2, v[0:1]
	v_mov_b32_e32 v0, v5
	v_mov_b32_e32 v1, v6
	v_pk_mul_f32 v[0:1], v[124:125], v[0:1] op_sel_hi:[0,1]
	s_waitcnt lgkmcnt(9)
	v_mfma_f32_32x32x16_f16 v[16:31], v[144:147], v[112:115], v[16:31]
	v_fma_mixlo_f16 v2, v124, v4, 0
	v_cvt_pk_f16_f32 v1, v0, v1
	v_pack_b32_f16 v0, v2, v1
	v_fma_mixlo_f16 v2, v124, v7, 0
	v_alignbit_b32 v1, v2, v1, 16
	v_bitop3_b32 v2, v164, v120, 1 bitop3:0x36
	v_lshl_or_b32 v2, v2, 4, v121
	s_waitcnt lgkmcnt(7)
	v_mfma_f32_32x32x16_f16 v[16:31], v[148:151], v[108:111], v[16:31]
	ds_write_b64 v2, v[0:1]
	v_mov_b32_e32 v0, v9
	v_mov_b32_e32 v1, v10
	v_mul_f32_e64 v0, v124, v0
	v_mul_f32_e64 v1, v124, v1
	v_fma_mixlo_f16 v2, v124, v8, 0
	v_cvt_pk_f16_f32 v1, v0, v1
	v_pack_b32_f16 v0, v2, v1
	s_waitcnt lgkmcnt(6)
	v_mfma_f32_32x32x16_f16 v[16:31], v[152:155], v[104:107], v[16:31]
	v_fma_mixlo_f16 v2, v124, v11, 0
	v_alignbit_b32 v1, v2, v1, 16
	v_bitop3_b32 v2, v164, v120, 2 bitop3:0x36
	v_lshl_or_b32 v2, v2, 4, v121
	ds_write_b64 v2, v[0:1]
	v_mov_b32_e32 v0, v13
	v_mov_b32_e32 v1, v14
	s_waitcnt lgkmcnt(5)
	v_mfma_f32_32x32x16_f16 v[16:31], v[156:159], v[96:99], v[16:31]
	v_mul_f32_e64 v0, v124, v0
	v_mul_f32_e64 v1, v124, v1
	v_fma_mixlo_f16 v2, v124, v12, 0
	v_cvt_pk_f16_f32 v1, v0, v1
	v_pack_b32_f16 v0, v2, v1
	v_fma_mixlo_f16 v2, v124, v15, 0
	v_alignbit_b32 v1, v2, v1, 16
	v_bitop3_b32 v2, v164, v120, 3 bitop3:0x36
	s_waitcnt lgkmcnt(3)
	v_mfma_f32_32x32x16_f16 v[16:31], v[160:163], v[100:103], v[16:31]
	v_lshl_or_b32 v2, v2, 4, v121
	ds_write_b64 v2, v[0:1]
	s_nop 9
	v_mov_b32_e32 v0, v17
	v_mov_b32_e32 v1, v18
	v_pk_mul_f32 v[0:1], v[124:125], v[0:1] op_sel_hi:[0,1]
	v_fma_mixlo_f16 v2, v124, v16, 0
	v_cvt_pk_f16_f32 v1, v0, v1
	v_pack_b32_f16 v0, v2, v1
	v_fma_mixlo_f16 v2, v124, v19, 0
	v_alignbit_b32 v1, v2, v1, 16
	v_bitop3_b32 v2, v164, v120, 4 bitop3:0x36
	v_lshl_or_b32 v2, v2, 4, v121
	ds_write_b64 v2, v[0:1]
	v_mov_b32_e32 v0, v21
	v_mov_b32_e32 v1, v22
	v_pk_mul_f32 v[0:1], v[124:125], v[0:1] op_sel_hi:[0,1]
	v_fma_mixlo_f16 v2, v124, v20, 0
	v_cvt_pk_f16_f32 v1, v0, v1
	v_pack_b32_f16 v0, v2, v1
	v_fma_mixlo_f16 v2, v124, v23, 0
	v_alignbit_b32 v1, v2, v1, 16
	v_bitop3_b32 v2, v164, v120, 5 bitop3:0x36
	v_lshl_or_b32 v2, v2, 4, v121
	ds_write_b64 v2, v[0:1]
	v_mov_b32_e32 v0, v25
	v_mov_b32_e32 v1, v26
	v_pk_mul_f32 v[0:1], v[124:125], v[0:1] op_sel_hi:[0,1]
	v_fma_mixlo_f16 v2, v124, v24, 0
	v_cvt_pk_f16_f32 v1, v0, v1
	v_pack_b32_f16 v0, v2, v1
	v_fma_mixlo_f16 v2, v124, v27, 0
	v_alignbit_b32 v1, v2, v1, 16
	v_bitop3_b32 v2, v164, v120, 6 bitop3:0x36
	v_lshl_or_b32 v2, v2, 4, v121
	ds_write_b64 v2, v[0:1]
	v_mov_b32_e32 v0, v29
	v_mov_b32_e32 v1, v30
	v_pk_mul_f32 v[0:1], v[124:125], v[0:1] op_sel_hi:[0,1]
	v_fma_mixlo_f16 v2, v124, v28, 0
	v_cvt_pk_f16_f32 v1, v0, v1
	v_pack_b32_f16 v0, v2, v1
	v_fma_mixlo_f16 v2, v124, v31, 0
	v_alignbit_b32 v1, v2, v1, 16
	v_bitop3_b32 v2, v164, v120, 7 bitop3:0x36
	v_lshl_or_b32 v2, v2, 4, v121
	ds_write_b64 v2, v[0:1]
	v_lshl_add_u64 v[0:1], s[0:1], 0, v[172:173]
	v_lshlrev_b32_e32 v172, 2, v127
	v_lshl_add_u64 v[0:1], v[0:1], 0, v[172:173]
	s_waitcnt lgkmcnt(0)
	s_barrier
	v_and_b32_e32 v245, 15, v116
	v_lshrrev_b32_e32 v246, 4, v116
	v_lshl_or_b32 v246, v119, 1, v246
	v_lshrrev_b32_e32 v250, 5, v126
	v_and_b32_e32 v250, 7, v250
	v_and_b32_e32 v247, 1, v246
	v_lshrrev_b32_e32 v248, 1, v246
	v_xor_b32_e32 v248, v248, v247
	v_lshl_or_b32 v247, v247, 1, v248
	v_and_b32_e32 v248, 3, v245
	v_lshrrev_b32_e32 v249, 2, v245
	v_lshl_or_b32 v248, v248, 2, v249
	v_xor_b32_e32 v247, v247, v248
	v_lshlrev_b32_e32 v240, 8, v245
	v_lshl_or_b32 v240, v247, 4, v240
	v_add_u32_e32 v240, 0x18000, v240
	v_xor_b32_e32 v241, 64, v240
	v_xor_b32_e32 v242, 0x80, v240
	v_xor_b32_e32 v243, 0xc0, v240
	v_lshlrev_b32_e32 v249, 7, v250
	v_lshl_or_b32 v249, v246, 4, v249
	v_and_b32_e32 v249, 0x3f0, v249
	global_load_dwordx4 v[96:99], v249, s[0:1]
	global_load_dwordx4 v[100:103], v249, s[0:1] offset:64
	v_lshlrev_b32_e32 v244, 19, v250
	v_lshl_or_b32 v244, v246, 16, v244
	v_lshl_or_b32 v244, v245, 3, v244
	v_and_b32_e32 v244, 0x3fff78, v244
	s_lshl_b64 s[22:23], s[2:3], 22
	s_add_u32 s22, s22, s12
	s_addc_u32 s23, s23, s13
	s_lshl_b32 s24, s14, 3
	s_add_u32 s22, s22, s24
	s_addc_u32 s23, s23, 0
	ds_read_b128 v[112:115], v240
	ds_read_b128 v[144:147], v240 offset:8192
	ds_read_b128 v[116:119], v241
	ds_read_b128 v[148:151], v241 offset:8192
	ds_read_b128 v[120:123], v242
	ds_read_b128 v[152:155], v242 offset:8192
	ds_read_b128 v[124:127], v243
	ds_read_b128 v[156:159], v243 offset:8192
	ds_read_b128 v[128:131], v240 offset:16384
	ds_read_b128 v[160:163], v240 offset:24576
	ds_read_b128 v[132:135], v241 offset:16384
	ds_read_b128 v[164:167], v241 offset:24576
	ds_read_b128 v[136:139], v242 offset:16384
	ds_read_b128 v[168:171], v242 offset:24576
	ds_read_b128 v[140:143], v243 offset:16384
	ds_read_b128 v[172:175], v243 offset:24576
	s_waitcnt vmcnt(2)
	s_waitcnt lgkmcnt(14)
	v_mfma_f32_16x16x32_f16 v[0:3], v[36:39], v[112:115], 0
	v_mfma_f32_16x16x32_f16 v[4:7], v[36:39], v[144:147], 0
	v_mfma_f32_16x16x32_f16 v[8:11], v[76:79], v[112:115], 0
	v_mfma_f32_16x16x32_f16 v[12:15], v[76:79], v[144:147], 0
	ds_read_b128 v[176:179], v240 offset:4096
	ds_read_b128 v[208:211], v240 offset:12288
	s_waitcnt lgkmcnt(14)
	v_mfma_f32_16x16x32_f16 v[0:3], v[32:35], v[116:119], v[0:3]
	v_mfma_f32_16x16x32_f16 v[4:7], v[32:35], v[148:151], v[4:7]
	v_mfma_f32_16x16x32_f16 v[8:11], v[72:75], v[116:119], v[8:11]
	v_mfma_f32_16x16x32_f16 v[12:15], v[72:75], v[148:151], v[12:15]
	ds_read_b128 v[180:183], v241 offset:4096
	ds_read_b128 v[212:215], v241 offset:12288
	s_waitcnt lgkmcnt(14)
	v_mfma_f32_16x16x32_f16 v[0:3], v[64:67], v[120:123], v[0:3]
	v_mfma_f32_16x16x32_f16 v[4:7], v[64:67], v[152:155], v[4:7]
	v_mfma_f32_16x16x32_f16 v[8:11], v[68:71], v[120:123], v[8:11]
	v_mfma_f32_16x16x32_f16 v[12:15], v[68:71], v[152:155], v[12:15]
	ds_read_b128 v[184:187], v242 offset:4096
	ds_read_b128 v[216:219], v242 offset:12288
	s_waitcnt lgkmcnt(14)
	v_mfma_f32_16x16x32_f16 v[0:3], v[48:51], v[124:127], v[0:3]
	v_mfma_f32_16x16x32_f16 v[4:7], v[48:51], v[156:159], v[4:7]
	v_mfma_f32_16x16x32_f16 v[8:11], v[52:55], v[124:127], v[8:11]
	v_mfma_f32_16x16x32_f16 v[12:15], v[52:55], v[156:159], v[12:15]
	ds_read_b128 v[188:191], v243 offset:4096
	ds_read_b128 v[220:223], v243 offset:12288
	s_waitcnt lgkmcnt(14)
	v_mfma_f32_16x16x32_f16 v[0:3], v[92:95], v[128:131], v[0:3]
	v_mfma_f32_16x16x32_f16 v[4:7], v[92:95], v[160:163], v[4:7]
	v_mfma_f32_16x16x32_f16 v[8:11], v[60:63], v[128:131], v[8:11]
	v_mfma_f32_16x16x32_f16 v[12:15], v[60:63], v[160:163], v[12:15]
	ds_read_b128 v[192:195], v240 offset:20480
	ds_read_b128 v[224:227], v240 offset:28672
	s_waitcnt lgkmcnt(14)
	v_mfma_f32_16x16x32_f16 v[0:3], v[84:87], v[132:135], v[0:3]
	v_mfma_f32_16x16x32_f16 v[4:7], v[84:87], v[164:167], v[4:7]
	v_mfma_f32_16x16x32_f16 v[8:11], v[56:59], v[132:135], v[8:11]
	v_mfma_f32_16x16x32_f16 v[12:15], v[56:59], v[164:167], v[12:15]
	ds_read_b128 v[196:199], v241 offset:20480
	ds_read_b128 v[228:231], v241 offset:28672
	s_waitcnt lgkmcnt(14)
	v_mfma_f32_16x16x32_f16 v[0:3], v[80:83], v[136:139], v[0:3]
	v_mfma_f32_16x16x32_f16 v[4:7], v[80:83], v[168:171], v[4:7]
	v_mfma_f32_16x16x32_f16 v[8:11], v[44:47], v[136:139], v[8:11]
	v_mfma_f32_16x16x32_f16 v[12:15], v[44:47], v[168:171], v[12:15]
	ds_read_b128 v[200:203], v242 offset:20480
	ds_read_b128 v[232:235], v242 offset:28672
	s_waitcnt lgkmcnt(14)
	v_mfma_f32_16x16x32_f16 v[0:3], v[88:91], v[140:143], v[0:3]
	v_mfma_f32_16x16x32_f16 v[4:7], v[88:91], v[172:175], v[4:7]
	v_mfma_f32_16x16x32_f16 v[8:11], v[40:43], v[140:143], v[8:11]
	v_mfma_f32_16x16x32_f16 v[12:15], v[40:43], v[172:175], v[12:15]
	ds_read_b128 v[204:207], v243 offset:20480
	ds_read_b128 v[236:239], v243 offset:28672
	s_waitcnt vmcnt(0)
	s_waitcnt lgkmcnt(14)
	v_mfma_f32_16x16x32_f16 v[16:19], v[36:39], v[176:179], 0
	v_mfma_f32_16x16x32_f16 v[20:23], v[36:39], v[208:211], 0
	v_mfma_f32_16x16x32_f16 v[24:27], v[76:79], v[176:179], 0
	v_mfma_f32_16x16x32_f16 v[28:31], v[76:79], v[208:211], 0
	s_add_u32 s26, s22, 0x0
	s_addc_u32 s27, s23, 0
	v_add_f32_e32 v104, v0, v96
	v_add_f32_e32 v105, v4, v96
	global_store_dwordx2 v244, v[104:105], s[26:27] nt
	s_waitcnt lgkmcnt(12)
	v_mfma_f32_16x16x32_f16 v[16:19], v[32:35], v[180:183], v[16:19]
	v_mfma_f32_16x16x32_f16 v[20:23], v[32:35], v[212:215], v[20:23]
	v_mfma_f32_16x16x32_f16 v[24:27], v[72:75], v[180:183], v[24:27]
	v_mfma_f32_16x16x32_f16 v[28:31], v[72:75], v[212:215], v[28:31]
	s_add_u32 s26, s22, 0x4000
	s_addc_u32 s27, s23, 0
	v_add_f32_e32 v106, v1, v97
	v_add_f32_e32 v107, v5, v97
	global_store_dwordx2 v244, v[106:107], s[26:27] nt
	s_waitcnt lgkmcnt(10)
	v_mfma_f32_16x16x32_f16 v[16:19], v[64:67], v[184:187], v[16:19]
	v_mfma_f32_16x16x32_f16 v[20:23], v[64:67], v[216:219], v[20:23]
	v_mfma_f32_16x16x32_f16 v[24:27], v[68:71], v[184:187], v[24:27]
	v_mfma_f32_16x16x32_f16 v[28:31], v[68:71], v[216:219], v[28:31]
	s_add_u32 s26, s22, 0x8000
	s_addc_u32 s27, s23, 0
	v_add_f32_e32 v108, v2, v98
	v_add_f32_e32 v109, v6, v98
	global_store_dwordx2 v244, v[108:109], s[26:27] nt
	s_waitcnt lgkmcnt(8)
	v_mfma_f32_16x16x32_f16 v[16:19], v[48:51], v[188:191], v[16:19]
	v_mfma_f32_16x16x32_f16 v[20:23], v[48:51], v[220:223], v[20:23]
	v_mfma_f32_16x16x32_f16 v[24:27], v[52:55], v[188:191], v[24:27]
	v_mfma_f32_16x16x32_f16 v[28:31], v[52:55], v[220:223], v[28:31]
	s_add_u32 s26, s22, 0xc000
	s_addc_u32 s27, s23, 0
	v_add_f32_e32 v110, v3, v99
	v_add_f32_e32 v111, v7, v99
	global_store_dwordx2 v244, v[110:111], s[26:27] nt
	s_waitcnt lgkmcnt(6)
	v_mfma_f32_16x16x32_f16 v[16:19], v[92:95], v[192:195], v[16:19]
	v_mfma_f32_16x16x32_f16 v[20:23], v[92:95], v[224:227], v[20:23]
	v_mfma_f32_16x16x32_f16 v[24:27], v[60:63], v[192:195], v[24:27]
	v_mfma_f32_16x16x32_f16 v[28:31], v[60:63], v[224:227], v[28:31]
	s_add_u32 s26, s22, 0x40000
	s_addc_u32 s27, s23, 0
	v_add_f32_e32 v104, v8, v100
	v_add_f32_e32 v105, v12, v100
	global_store_dwordx2 v244, v[104:105], s[26:27] nt
	s_waitcnt lgkmcnt(4)
	v_mfma_f32_16x16x32_f16 v[16:19], v[84:87], v[196:199], v[16:19]
	v_mfma_f32_16x16x32_f16 v[20:23], v[84:87], v[228:231], v[20:23]
	v_mfma_f32_16x16x32_f16 v[24:27], v[56:59], v[196:199], v[24:27]
	v_mfma_f32_16x16x32_f16 v[28:31], v[56:59], v[228:231], v[28:31]
	s_add_u32 s26, s22, 0x44000
	s_addc_u32 s27, s23, 0
	v_add_f32_e32 v106, v9, v101
	v_add_f32_e32 v107, v13, v101
	global_store_dwordx2 v244, v[106:107], s[26:27] nt
	s_waitcnt lgkmcnt(2)
	v_mfma_f32_16x16x32_f16 v[16:19], v[80:83], v[200:203], v[16:19]
	v_mfma_f32_16x16x32_f16 v[20:23], v[80:83], v[232:235], v[20:23]
	v_mfma_f32_16x16x32_f16 v[24:27], v[44:47], v[200:203], v[24:27]
	v_mfma_f32_16x16x32_f16 v[28:31], v[44:47], v[232:235], v[28:31]
	s_add_u32 s26, s22, 0x48000
	s_addc_u32 s27, s23, 0
	v_add_f32_e32 v108, v10, v102
	v_add_f32_e32 v109, v14, v102
	global_store_dwordx2 v244, v[108:109], s[26:27] nt
	s_waitcnt lgkmcnt(0)
	v_mfma_f32_16x16x32_f16 v[16:19], v[88:91], v[204:207], v[16:19]
	v_mfma_f32_16x16x32_f16 v[20:23], v[88:91], v[236:239], v[20:23]
	v_mfma_f32_16x16x32_f16 v[24:27], v[40:43], v[204:207], v[24:27]
	v_mfma_f32_16x16x32_f16 v[28:31], v[40:43], v[236:239], v[28:31]
	s_add_u32 s26, s22, 0x4c000
	s_addc_u32 s27, s23, 0
	v_add_f32_e32 v110, v11, v103
	v_add_f32_e32 v111, v15, v103
	global_store_dwordx2 v244, v[110:111], s[26:27] nt
	s_nop 7
	s_nop 1
	s_add_u32 s26, s22, 0x0
	s_addc_u32 s27, s23, 0
	v_add_f32_e32 v104, v16, v96
	v_add_f32_e32 v105, v20, v96
	global_store_dwordx2 v244, v[104:105], s[26:27] offset:128 nt
	s_add_u32 s26, s22, 0x4000
	s_addc_u32 s27, s23, 0
	v_add_f32_e32 v106, v17, v97
	v_add_f32_e32 v107, v21, v97
	global_store_dwordx2 v244, v[106:107], s[26:27] offset:128 nt
	s_add_u32 s26, s22, 0x8000
	s_addc_u32 s27, s23, 0
	v_add_f32_e32 v108, v18, v98
	v_add_f32_e32 v109, v22, v98
	global_store_dwordx2 v244, v[108:109], s[26:27] offset:128 nt
	s_add_u32 s26, s22, 0xc000
	s_addc_u32 s27, s23, 0
	v_add_f32_e32 v110, v19, v99
	v_add_f32_e32 v111, v23, v99
	global_store_dwordx2 v244, v[110:111], s[26:27] offset:128 nt
	s_add_u32 s26, s22, 0x40000
	s_addc_u32 s27, s23, 0
	v_add_f32_e32 v104, v24, v100
	v_add_f32_e32 v105, v28, v100
	global_store_dwordx2 v244, v[104:105], s[26:27] offset:128 nt
	s_add_u32 s26, s22, 0x44000
	s_addc_u32 s27, s23, 0
	v_add_f32_e32 v106, v25, v101
	v_add_f32_e32 v107, v29, v101
	global_store_dwordx2 v244, v[106:107], s[26:27] offset:128 nt
	s_add_u32 s26, s22, 0x48000
	s_addc_u32 s27, s23, 0
	v_add_f32_e32 v108, v26, v102
	v_add_f32_e32 v109, v30, v102
	global_store_dwordx2 v244, v[108:109], s[26:27] offset:128 nt
	s_add_u32 s26, s22, 0x4c000
	s_addc_u32 s27, s23, 0
	v_add_f32_e32 v110, v27, v103
	v_add_f32_e32 v111, v31, v103
	global_store_dwordx2 v244, v[110:111], s[26:27] offset:128 nt
	s_endpgm
